# FFN-up epilogue rewritten by hand with packed f32 math (v_pk_mul/v_pk_fma in place on the accumulators), no zero-init movs, one 64-bit add per row group for the store address
# speedup vs baseline: 1.0352x; 1.0088x over previous
.LBB0_968:
	s_mov_b32 s4, 0xbc800000
	s_mov_b32 s0, 0x45800000
	s_movk_i32 s19, 0xb00
	v_mov_b32_e32 v24, 0x43e00000
	v_ashrrev_i32_e32 v3, 2, v0
	v_lshrrev_b32_e32 v2, 1, v0
	v_and_b32_e32 v3, 0xffffffc0, v3
	v_and_b32_e32 v2, 0x78, v2
	v_lshl_add_u32 v3, s55, 8, v3
	v_lshl_or_b32 v2, s59, 7, v2
	v_and_or_b32 v6, v0, 15, v3
	v_mov_b64_e32 v[4:5], s[14:15]
	v_ashrrev_i32_e32 v3, 31, v2
	v_mov_b32_e32 v12, 0xb000
	v_mov_b32_e32 v13, 0
	v_mad_i64_i32 v[10:11], vcc, v6, s19, v[4:5]
	v_lshl_add_u64 v[10:11], v[10:11], 0, v[2:3]
	v_pk_mul_f32 v[154:155], v[146:147], v[154:155]
	v_pk_mul_f32 v[156:157], v[148:149], v[156:157]
	v_pk_mul_f32 v[150:151], v[158:159], v[150:151]
	v_pk_mul_f32 v[152:153], v[160:161], v[152:153]
	v_pk_mul_f32 v[146:147], v[146:147], s[4:5] op_sel_hi:[1,0]
	v_pk_mul_f32 v[148:149], v[148:149], s[4:5] op_sel_hi:[1,0]
	v_pk_mul_f32 v[158:159], v[158:159], s[4:5] op_sel_hi:[1,0]
	v_pk_mul_f32 v[160:161], v[160:161], s[4:5] op_sel_hi:[1,0]
	v_exp_f32_e32 v146, v146
	v_exp_f32_e32 v147, v147
	v_exp_f32_e32 v148, v148
	v_exp_f32_e32 v149, v149
	v_exp_f32_e32 v158, v158
	v_exp_f32_e32 v159, v159
	v_exp_f32_e32 v160, v160
	v_exp_f32_e32 v161, v161
	v_pk_fma_f32 v[146:147], v[146:147], s[0:1], s[0:1] op_sel_hi:[1,0,0]
	v_pk_fma_f32 v[148:149], v[148:149], s[0:1], s[0:1] op_sel_hi:[1,0,0]
	v_pk_fma_f32 v[158:159], v[158:159], s[0:1], s[0:1] op_sel_hi:[1,0,0]
	v_pk_fma_f32 v[160:161], v[160:161], s[0:1], s[0:1] op_sel_hi:[1,0,0]
	v_rcp_f32_e32 v146, v146
	v_rcp_f32_e32 v147, v147
	v_rcp_f32_e32 v148, v148
	v_rcp_f32_e32 v149, v149
	v_rcp_f32_e32 v158, v158
	v_rcp_f32_e32 v159, v159
	v_rcp_f32_e32 v160, v160
	v_rcp_f32_e32 v161, v161
	v_pk_mul_f32 v[154:155], v[154:155], v[146:147]
	v_pk_mul_f32 v[156:157], v[156:157], v[148:149]
	v_pk_mul_f32 v[150:151], v[150:151], v[158:159]
	v_pk_mul_f32 v[152:153], v[152:153], v[160:161]
	v_med3_f32 v154, v154, s35, v24
	v_med3_f32 v155, v155, s35, v24
	v_med3_f32 v156, v156, s35, v24
	v_med3_f32 v157, v157, s35, v24
	v_med3_f32 v150, v150, s35, v24
	v_med3_f32 v151, v151, s35, v24
	v_med3_f32 v152, v152, s35, v24
	v_med3_f32 v153, v153, s35, v24
	v_cvt_pk_fp8_f32 v146, v154, v155
	v_cvt_pk_fp8_f32 v147, v150, v151
	v_cvt_pk_fp8_f32 v146, v156, v157 op_sel:[0,0,1]
	v_cvt_pk_fp8_f32 v147, v152, v153 op_sel:[0,0,1]
	v_mov_b64_e32 v[16:17], v[10:11]
	global_store_dwordx2 v[16:17], v[146:147], off
	v_pk_mul_f32 v[134:135], v[142:143], v[134:135]
	v_pk_mul_f32 v[136:137], v[144:145], v[136:137]
	v_pk_mul_f32 v[130:131], v[138:139], v[130:131]
	v_pk_mul_f32 v[132:133], v[140:141], v[132:133]
	v_pk_mul_f32 v[142:143], v[142:143], s[4:5] op_sel_hi:[1,0]
	v_pk_mul_f32 v[144:145], v[144:145], s[4:5] op_sel_hi:[1,0]
	v_pk_mul_f32 v[138:139], v[138:139], s[4:5] op_sel_hi:[1,0]
	v_pk_mul_f32 v[140:141], v[140:141], s[4:5] op_sel_hi:[1,0]
	v_exp_f32_e32 v142, v142
	v_exp_f32_e32 v143, v143
	v_exp_f32_e32 v144, v144
	v_exp_f32_e32 v145, v145
	v_exp_f32_e32 v138, v138
	v_exp_f32_e32 v139, v139
	v_exp_f32_e32 v140, v140
	v_exp_f32_e32 v141, v141
	v_pk_fma_f32 v[142:143], v[142:143], s[0:1], s[0:1] op_sel_hi:[1,0,0]
	v_pk_fma_f32 v[144:145], v[144:145], s[0:1], s[0:1] op_sel_hi:[1,0,0]
	v_pk_fma_f32 v[138:139], v[138:139], s[0:1], s[0:1] op_sel_hi:[1,0,0]
	v_pk_fma_f32 v[140:141], v[140:141], s[0:1], s[0:1] op_sel_hi:[1,0,0]
	v_rcp_f32_e32 v142, v142
	v_rcp_f32_e32 v143, v143
	v_rcp_f32_e32 v144, v144
	v_rcp_f32_e32 v145, v145
	v_rcp_f32_e32 v138, v138
	v_rcp_f32_e32 v139, v139
	v_rcp_f32_e32 v140, v140
	v_rcp_f32_e32 v141, v141
	v_pk_mul_f32 v[134:135], v[134:135], v[142:143]
	v_pk_mul_f32 v[136:137], v[136:137], v[144:145]
	v_pk_mul_f32 v[130:131], v[130:131], v[138:139]
	v_pk_mul_f32 v[132:133], v[132:133], v[140:141]
	v_med3_f32 v134, v134, s35, v24
	v_med3_f32 v135, v135, s35, v24
	v_med3_f32 v136, v136, s35, v24
	v_med3_f32 v137, v137, s35, v24
	v_med3_f32 v130, v130, s35, v24
	v_med3_f32 v131, v131, s35, v24
	v_med3_f32 v132, v132, s35, v24
	v_med3_f32 v133, v133, s35, v24
	v_cvt_pk_fp8_f32 v142, v134, v135
	v_cvt_pk_fp8_f32 v143, v130, v131
	v_cvt_pk_fp8_f32 v142, v136, v137 op_sel:[0,0,1]
	v_cvt_pk_fp8_f32 v143, v132, v133 op_sel:[0,0,1]
	v_lshl_add_u64 v[16:17], v[16:17], 0, v[12:13]
	global_store_dwordx2 v[16:17], v[142:143], off
	v_pk_mul_f32 v[118:119], v[126:127], v[118:119]
	v_pk_mul_f32 v[120:121], v[128:129], v[120:121]
	v_pk_mul_f32 v[114:115], v[122:123], v[114:115]
	v_pk_mul_f32 v[116:117], v[124:125], v[116:117]
	v_pk_mul_f32 v[126:127], v[126:127], s[4:5] op_sel_hi:[1,0]
	v_pk_mul_f32 v[128:129], v[128:129], s[4:5] op_sel_hi:[1,0]
	v_pk_mul_f32 v[122:123], v[122:123], s[4:5] op_sel_hi:[1,0]
	v_pk_mul_f32 v[124:125], v[124:125], s[4:5] op_sel_hi:[1,0]
	v_exp_f32_e32 v126, v126
	v_exp_f32_e32 v127, v127
	v_exp_f32_e32 v128, v128
	v_exp_f32_e32 v129, v129
	v_exp_f32_e32 v122, v122
	v_exp_f32_e32 v123, v123
	v_exp_f32_e32 v124, v124
	v_exp_f32_e32 v125, v125
	v_pk_fma_f32 v[126:127], v[126:127], s[0:1], s[0:1] op_sel_hi:[1,0,0]
	v_pk_fma_f32 v[128:129], v[128:129], s[0:1], s[0:1] op_sel_hi:[1,0,0]
	v_pk_fma_f32 v[122:123], v[122:123], s[0:1], s[0:1] op_sel_hi:[1,0,0]
	v_pk_fma_f32 v[124:125], v[124:125], s[0:1], s[0:1] op_sel_hi:[1,0,0]
	v_rcp_f32_e32 v126, v126
	v_rcp_f32_e32 v127, v127
	v_rcp_f32_e32 v128, v128
	v_rcp_f32_e32 v129, v129
	v_rcp_f32_e32 v122, v122
	v_rcp_f32_e32 v123, v123
	v_rcp_f32_e32 v124, v124
	v_rcp_f32_e32 v125, v125
	v_pk_mul_f32 v[118:119], v[118:119], v[126:127]
	v_pk_mul_f32 v[120:121], v[120:121], v[128:129]
	v_pk_mul_f32 v[114:115], v[114:115], v[122:123]
	v_pk_mul_f32 v[116:117], v[116:117], v[124:125]
	v_med3_f32 v118, v118, s35, v24
	v_med3_f32 v119, v119, s35, v24
	v_med3_f32 v120, v120, s35, v24
	v_med3_f32 v121, v121, s35, v24
	v_med3_f32 v114, v114, s35, v24
	v_med3_f32 v115, v115, s35, v24
	v_med3_f32 v116, v116, s35, v24
	v_med3_f32 v117, v117, s35, v24
	v_cvt_pk_fp8_f32 v126, v118, v119
	v_cvt_pk_fp8_f32 v127, v114, v115
	v_cvt_pk_fp8_f32 v126, v120, v121 op_sel:[0,0,1]
	v_cvt_pk_fp8_f32 v127, v116, v117 op_sel:[0,0,1]
	v_lshl_add_u64 v[16:17], v[16:17], 0, v[12:13]
	global_store_dwordx2 v[16:17], v[126:127], off
	v_pk_mul_f32 v[102:103], v[110:111], v[102:103]
	v_pk_mul_f32 v[104:105], v[112:113], v[104:105]
	v_pk_mul_f32 v[98:99], v[106:107], v[98:99]
	v_pk_mul_f32 v[100:101], v[108:109], v[100:101]
	v_pk_mul_f32 v[110:111], v[110:111], s[4:5] op_sel_hi:[1,0]
	v_pk_mul_f32 v[112:113], v[112:113], s[4:5] op_sel_hi:[1,0]
	v_pk_mul_f32 v[106:107], v[106:107], s[4:5] op_sel_hi:[1,0]
	v_pk_mul_f32 v[108:109], v[108:109], s[4:5] op_sel_hi:[1,0]
	v_exp_f32_e32 v110, v110
	v_exp_f32_e32 v111, v111
	v_exp_f32_e32 v112, v112
	v_exp_f32_e32 v113, v113
	v_exp_f32_e32 v106, v106
	v_exp_f32_e32 v107, v107
	v_exp_f32_e32 v108, v108
	v_exp_f32_e32 v109, v109
	v_pk_fma_f32 v[110:111], v[110:111], s[0:1], s[0:1] op_sel_hi:[1,0,0]
	v_pk_fma_f32 v[112:113], v[112:113], s[0:1], s[0:1] op_sel_hi:[1,0,0]
	v_pk_fma_f32 v[106:107], v[106:107], s[0:1], s[0:1] op_sel_hi:[1,0,0]
	v_pk_fma_f32 v[108:109], v[108:109], s[0:1], s[0:1] op_sel_hi:[1,0,0]
	v_rcp_f32_e32 v110, v110
	v_rcp_f32_e32 v111, v111
	v_rcp_f32_e32 v112, v112
	v_rcp_f32_e32 v113, v113
	v_rcp_f32_e32 v106, v106
	v_rcp_f32_e32 v107, v107
	v_rcp_f32_e32 v108, v108
	v_rcp_f32_e32 v109, v109
	v_pk_mul_f32 v[102:103], v[102:103], v[110:111]
	v_pk_mul_f32 v[104:105], v[104:105], v[112:113]
	v_pk_mul_f32 v[98:99], v[98:99], v[106:107]
	v_pk_mul_f32 v[100:101], v[100:101], v[108:109]
	v_med3_f32 v102, v102, s35, v24
	v_med3_f32 v103, v103, s35, v24
	v_med3_f32 v104, v104, s35, v24
	v_med3_f32 v105, v105, s35, v24
	v_med3_f32 v98, v98, s35, v24
	v_med3_f32 v99, v99, s35, v24
	v_med3_f32 v100, v100, s35, v24
	v_med3_f32 v101, v101, s35, v24
	v_cvt_pk_fp8_f32 v110, v102, v103
	v_cvt_pk_fp8_f32 v111, v98, v99
	v_cvt_pk_fp8_f32 v110, v104, v105 op_sel:[0,0,1]
	v_cvt_pk_fp8_f32 v111, v100, v101 op_sel:[0,0,1]
	v_lshl_add_u64 v[16:17], v[16:17], 0, v[12:13]
	global_store_dwordx2 v[16:17], v[110:111], off
	v_pk_mul_f32 v[86:87], v[94:95], v[86:87]
	v_pk_mul_f32 v[88:89], v[96:97], v[88:89]
	v_pk_mul_f32 v[82:83], v[90:91], v[82:83]
	v_pk_mul_f32 v[84:85], v[92:93], v[84:85]
	v_pk_mul_f32 v[94:95], v[94:95], s[4:5] op_sel_hi:[1,0]
	v_pk_mul_f32 v[96:97], v[96:97], s[4:5] op_sel_hi:[1,0]
	v_pk_mul_f32 v[90:91], v[90:91], s[4:5] op_sel_hi:[1,0]
	v_pk_mul_f32 v[92:93], v[92:93], s[4:5] op_sel_hi:[1,0]
	v_exp_f32_e32 v94, v94
	v_exp_f32_e32 v95, v95
	v_exp_f32_e32 v96, v96
	v_exp_f32_e32 v97, v97
	v_exp_f32_e32 v90, v90
	v_exp_f32_e32 v91, v91
	v_exp_f32_e32 v92, v92
	v_exp_f32_e32 v93, v93
	v_pk_fma_f32 v[94:95], v[94:95], s[0:1], s[0:1] op_sel_hi:[1,0,0]
	v_pk_fma_f32 v[96:97], v[96:97], s[0:1], s[0:1] op_sel_hi:[1,0,0]
	v_pk_fma_f32 v[90:91], v[90:91], s[0:1], s[0:1] op_sel_hi:[1,0,0]
	v_pk_fma_f32 v[92:93], v[92:93], s[0:1], s[0:1] op_sel_hi:[1,0,0]
	v_rcp_f32_e32 v94, v94
	v_rcp_f32_e32 v95, v95
	v_rcp_f32_e32 v96, v96
	v_rcp_f32_e32 v97, v97
	v_rcp_f32_e32 v90, v90
	v_rcp_f32_e32 v91, v91
	v_rcp_f32_e32 v92, v92
	v_rcp_f32_e32 v93, v93
	v_pk_mul_f32 v[86:87], v[86:87], v[94:95]
	v_pk_mul_f32 v[88:89], v[88:89], v[96:97]
	v_pk_mul_f32 v[82:83], v[82:83], v[90:91]
	v_pk_mul_f32 v[84:85], v[84:85], v[92:93]
	v_med3_f32 v86, v86, s35, v24
	v_med3_f32 v87, v87, s35, v24
	v_med3_f32 v88, v88, s35, v24
	v_med3_f32 v89, v89, s35, v24
	v_med3_f32 v82, v82, s35, v24
	v_med3_f32 v83, v83, s35, v24
	v_med3_f32 v84, v84, s35, v24
	v_med3_f32 v85, v85, s35, v24
	v_cvt_pk_fp8_f32 v94, v86, v87
	v_cvt_pk_fp8_f32 v95, v82, v83
	v_cvt_pk_fp8_f32 v94, v88, v89 op_sel:[0,0,1]
	v_cvt_pk_fp8_f32 v95, v84, v85 op_sel:[0,0,1]
	v_lshl_add_u64 v[16:17], v[12:13], 3, v[10:11]
	global_store_dwordx2 v[16:17], v[94:95], off
	v_pk_mul_f32 v[70:71], v[78:79], v[70:71]
	v_pk_mul_f32 v[72:73], v[80:81], v[72:73]
	v_pk_mul_f32 v[66:67], v[74:75], v[66:67]
	v_pk_mul_f32 v[68:69], v[76:77], v[68:69]
	v_pk_mul_f32 v[78:79], v[78:79], s[4:5] op_sel_hi:[1,0]
	v_pk_mul_f32 v[80:81], v[80:81], s[4:5] op_sel_hi:[1,0]
	v_pk_mul_f32 v[74:75], v[74:75], s[4:5] op_sel_hi:[1,0]
	v_pk_mul_f32 v[76:77], v[76:77], s[4:5] op_sel_hi:[1,0]
	v_exp_f32_e32 v78, v78
	v_exp_f32_e32 v79, v79
	v_exp_f32_e32 v80, v80
	v_exp_f32_e32 v81, v81
	v_exp_f32_e32 v74, v74
	v_exp_f32_e32 v75, v75
	v_exp_f32_e32 v76, v76
	v_exp_f32_e32 v77, v77
	v_pk_fma_f32 v[78:79], v[78:79], s[0:1], s[0:1] op_sel_hi:[1,0,0]
	v_pk_fma_f32 v[80:81], v[80:81], s[0:1], s[0:1] op_sel_hi:[1,0,0]
	v_pk_fma_f32 v[74:75], v[74:75], s[0:1], s[0:1] op_sel_hi:[1,0,0]
	v_pk_fma_f32 v[76:77], v[76:77], s[0:1], s[0:1] op_sel_hi:[1,0,0]
	v_rcp_f32_e32 v78, v78
	v_rcp_f32_e32 v79, v79
	v_rcp_f32_e32 v80, v80
	v_rcp_f32_e32 v81, v81
	v_rcp_f32_e32 v74, v74
	v_rcp_f32_e32 v75, v75
	v_rcp_f32_e32 v76, v76
	v_rcp_f32_e32 v77, v77
	v_pk_mul_f32 v[70:71], v[70:71], v[78:79]
	v_pk_mul_f32 v[72:73], v[72:73], v[80:81]
	v_pk_mul_f32 v[66:67], v[66:67], v[74:75]
	v_pk_mul_f32 v[68:69], v[68:69], v[76:77]
	v_med3_f32 v70, v70, s35, v24
	v_med3_f32 v71, v71, s35, v24
	v_med3_f32 v72, v72, s35, v24
	v_med3_f32 v73, v73, s35, v24
	v_med3_f32 v66, v66, s35, v24
	v_med3_f32 v67, v67, s35, v24
	v_med3_f32 v68, v68, s35, v24
	v_med3_f32 v69, v69, s35, v24
	v_cvt_pk_fp8_f32 v78, v70, v71
	v_cvt_pk_fp8_f32 v79, v66, v67
	v_cvt_pk_fp8_f32 v78, v72, v73 op_sel:[0,0,1]
	v_cvt_pk_fp8_f32 v79, v68, v69 op_sel:[0,0,1]
	v_lshl_add_u64 v[16:17], v[16:17], 0, v[12:13]
	global_store_dwordx2 v[16:17], v[78:79], off
	v_pk_mul_f32 v[54:55], v[62:63], v[54:55]
	v_pk_mul_f32 v[56:57], v[64:65], v[56:57]
	v_pk_mul_f32 v[50:51], v[58:59], v[50:51]
	v_pk_mul_f32 v[52:53], v[60:61], v[52:53]
	v_pk_mul_f32 v[62:63], v[62:63], s[4:5] op_sel_hi:[1,0]
	v_pk_mul_f32 v[64:65], v[64:65], s[4:5] op_sel_hi:[1,0]
	v_pk_mul_f32 v[58:59], v[58:59], s[4:5] op_sel_hi:[1,0]
	v_pk_mul_f32 v[60:61], v[60:61], s[4:5] op_sel_hi:[1,0]
	v_exp_f32_e32 v62, v62
	v_exp_f32_e32 v63, v63
	v_exp_f32_e32 v64, v64
	v_exp_f32_e32 v65, v65
	v_exp_f32_e32 v58, v58
	v_exp_f32_e32 v59, v59
	v_exp_f32_e32 v60, v60
	v_exp_f32_e32 v61, v61
	v_pk_fma_f32 v[62:63], v[62:63], s[0:1], s[0:1] op_sel_hi:[1,0,0]
	v_pk_fma_f32 v[64:65], v[64:65], s[0:1], s[0:1] op_sel_hi:[1,0,0]
	v_pk_fma_f32 v[58:59], v[58:59], s[0:1], s[0:1] op_sel_hi:[1,0,0]
	v_pk_fma_f32 v[60:61], v[60:61], s[0:1], s[0:1] op_sel_hi:[1,0,0]
	v_rcp_f32_e32 v62, v62
	v_rcp_f32_e32 v63, v63
	v_rcp_f32_e32 v64, v64
	v_rcp_f32_e32 v65, v65
	v_rcp_f32_e32 v58, v58
	v_rcp_f32_e32 v59, v59
	v_rcp_f32_e32 v60, v60
	v_rcp_f32_e32 v61, v61
	v_pk_mul_f32 v[54:55], v[54:55], v[62:63]
	v_pk_mul_f32 v[56:57], v[56:57], v[64:65]
	v_pk_mul_f32 v[50:51], v[50:51], v[58:59]
	v_pk_mul_f32 v[52:53], v[52:53], v[60:61]
	v_med3_f32 v54, v54, s35, v24
	v_med3_f32 v55, v55, s35, v24
	v_med3_f32 v56, v56, s35, v24
	v_med3_f32 v57, v57, s35, v24
	v_med3_f32 v50, v50, s35, v24
	v_med3_f32 v51, v51, s35, v24
	v_med3_f32 v52, v52, s35, v24
	v_med3_f32 v53, v53, s35, v24
	v_cvt_pk_fp8_f32 v62, v54, v55
	v_cvt_pk_fp8_f32 v63, v50, v51
	v_cvt_pk_fp8_f32 v62, v56, v57 op_sel:[0,0,1]
	v_cvt_pk_fp8_f32 v63, v52, v53 op_sel:[0,0,1]
	v_lshl_add_u64 v[16:17], v[16:17], 0, v[12:13]
	global_store_dwordx2 v[16:17], v[62:63], off
	v_pk_mul_f32 v[38:39], v[46:47], v[38:39]
	v_pk_mul_f32 v[40:41], v[48:49], v[40:41]
	v_pk_mul_f32 v[34:35], v[42:43], v[34:35]
	v_pk_mul_f32 v[36:37], v[44:45], v[36:37]
	v_pk_mul_f32 v[46:47], v[46:47], s[4:5] op_sel_hi:[1,0]
	v_pk_mul_f32 v[48:49], v[48:49], s[4:5] op_sel_hi:[1,0]
	v_pk_mul_f32 v[42:43], v[42:43], s[4:5] op_sel_hi:[1,0]
	v_pk_mul_f32 v[44:45], v[44:45], s[4:5] op_sel_hi:[1,0]
	v_exp_f32_e32 v46, v46
	v_exp_f32_e32 v47, v47
	v_exp_f32_e32 v48, v48
	v_exp_f32_e32 v49, v49
	v_exp_f32_e32 v42, v42
	v_exp_f32_e32 v43, v43
	v_exp_f32_e32 v44, v44
	v_exp_f32_e32 v45, v45
	v_pk_fma_f32 v[46:47], v[46:47], s[0:1], s[0:1] op_sel_hi:[1,0,0]
	v_pk_fma_f32 v[48:49], v[48:49], s[0:1], s[0:1] op_sel_hi:[1,0,0]
	v_pk_fma_f32 v[42:43], v[42:43], s[0:1], s[0:1] op_sel_hi:[1,0,0]
	v_pk_fma_f32 v[44:45], v[44:45], s[0:1], s[0:1] op_sel_hi:[1,0,0]
	v_rcp_f32_e32 v46, v46
	v_rcp_f32_e32 v47, v47
	v_rcp_f32_e32 v48, v48
	v_rcp_f32_e32 v49, v49
	v_rcp_f32_e32 v42, v42
	v_rcp_f32_e32 v43, v43
	v_rcp_f32_e32 v44, v44
	v_rcp_f32_e32 v45, v45
	v_pk_mul_f32 v[38:39], v[38:39], v[46:47]
	v_pk_mul_f32 v[40:41], v[40:41], v[48:49]
	v_pk_mul_f32 v[34:35], v[34:35], v[42:43]
	v_pk_mul_f32 v[36:37], v[36:37], v[44:45]
	v_med3_f32 v38, v38, s35, v24
	v_med3_f32 v39, v39, s35, v24
	v_med3_f32 v40, v40, s35, v24
	v_med3_f32 v41, v41, s35, v24
	v_med3_f32 v34, v34, s35, v24
	v_med3_f32 v35, v35, s35, v24
	v_med3_f32 v36, v36, s35, v24
	v_med3_f32 v37, v37, s35, v24
	v_cvt_pk_fp8_f32 v46, v38, v39
	v_cvt_pk_fp8_f32 v47, v34, v35
	v_cvt_pk_fp8_f32 v46, v40, v41 op_sel:[0,0,1]
	v_cvt_pk_fp8_f32 v47, v36, v37 op_sel:[0,0,1]
	v_lshl_add_u64 v[16:17], v[16:17], 0, v[12:13]
	s_and_b64 vcc, exec, s[2:3]
	s_mov_b64 s[0:1], -1
	global_store_dwordx2 v[16:17], v[46:47], off
	s_cbranch_vccnz .LBB0_952
	s_andn2_b64 vcc, exec, s[10:11]
	s_cbranch_vccnz .LBB0_951
	s_barrier
	s_branch .LBB0_951
